# baseline (speedup 1.0000x reference)
_Z11gram_kernelPKfPKiS0_S0_S0_S0_S0_S0_S0_S0_S0_Pf:
	s_load_dwordx4 s[24:27], s[0:1], 0x0
	s_load_dwordx2 s[28:29], s[0:1], 0x40
	s_load_dwordx4 s[20:23], s[0:1], 0x30
	s_load_dwordx2 s[10:11], s[0:1], 0x58
	s_load_dwordx2 s[44:45], s[0:1], 0x20
	s_load_dwordx2 s[68:69], s[0:1], 0x10
	s_load_dwordx2 s[60:61], s[0:1], 0x18
	s_load_dwordx2 s[62:63], s[0:1], 0x28
	s_load_dwordx2 s[64:65], s[0:1], 0x48
	s_load_dwordx2 s[66:67], s[0:1], 0x50
	s_ashr_i32 s30, s2, 1
	v_mov_b32_e32 v11, 0
	s_ashr_i32 s31, s30, 31
	s_lshl_b32 s46, s30, 11
	s_lshl_b32 s3, s2, 10
	s_ashr_i32 s47, s46, 31
	s_and_b32 s33, s3, 0x400
	v_lshlrev_b32_e32 v46, 2, v0
	v_mov_b32_e32 v47, 0
	v_lshlrev_b32_e32 v212, 1, v0
	v_mov_b32_e32 v213, v47
	v_lshrrev_b32_e32 v219, 6, v0
	v_bfe_u32 v214, v0, 5, 1
	v_and_b32_e32 v220, 31, v0
	s_or_b32 s3, s46, s33
	v_lshlrev_b32_e32 v216, 4, v219
	v_lshlrev_b32_e32 v221, 3, v214
	v_or3_b32 v1, s3, v216, v221
	v_lshlrev_b32_e32 v232, 4, v220
	v_and_b32_e32 v218, 63, v0
	s_mov_b32 s39, 0x20000
	s_brev_b32 s38, 16
	v_lshl_or_b32 v180, v1, 9, v232
	v_add_u32_e32 v1, 0x10000, v180
	s_lshl_b64 s[4:5], s[46:47], 2
	s_lshl_b32 s3, s33, 2
	s_lshl_b64 s[6:7], s[30:31], 14
	s_waitcnt lgkmcnt(0)
	s_add_u32 s48, s20, s6
	s_addc_u32 s49, s21, s7
	s_mov_b64 s[36:37], s[24:25]
	s_and_b32 s37, s37, 0xffff
	s_add_u32 s26, s26, s4
	s_addc_u32 s27, s27, s5
	s_add_u32 s26, s26, s3
	s_addc_u32 s27, s27, 0
	v_lshl_add_u64 v[32:33], v[212:213], 2, s[26:27]
	buffer_load_dwordx4 v[34:37], v180, s[36:39], 0 offen nt
	buffer_load_dwordx4 v[38:41], v180, s[36:39], 0 offen offset:512 nt
	buffer_load_dwordx4 v[42:45], v180, s[36:39], 0 offen offset:1024 nt
	buffer_load_dwordx4 v[96:99], v180, s[36:39], 0 offen offset:1536 nt
	buffer_load_dwordx4 v[100:103], v180, s[36:39], 0 offen offset:2048 nt
	buffer_load_dwordx4 v[104:107], v180, s[36:39], 0 offen offset:2560 nt
	buffer_load_dwordx4 v[108:111], v180, s[36:39], 0 offen offset:3072 nt
	buffer_load_dwordx4 v[112:115], v180, s[36:39], 0 offen offset:3584 nt
	global_load_dwordx2 v[32:33], v[32:33], off
	global_load_dword v250, v47, s[22:23]
	global_load_dword v250, v47, s[28:29]
	global_load_dword v250, v47, s[68:69]
	global_load_dword v250, v47, s[44:45]
	global_load_dword v250, v47, s[48:49]
	global_load_dword v250, v47, s[60:61]
	global_load_dword v250, v47, s[62:63]
	global_load_dword v250, v47, s[64:65]
	global_load_dword v250, v47, s[66:67]
	buffer_load_dwordx4 v[116:119], v1, s[36:39], 0 offen nt
	buffer_load_dwordx4 v[120:123], v1, s[36:39], 0 offen offset:512 nt
	buffer_load_dwordx4 v[124:127], v1, s[36:39], 0 offen offset:1024 nt
	buffer_load_dwordx4 v[128:131], v1, s[36:39], 0 offen offset:1536 nt
	buffer_load_dwordx4 v[132:135], v1, s[36:39], 0 offen offset:2048 nt
	buffer_load_dwordx4 v[136:139], v1, s[36:39], 0 offen offset:2560 nt
	buffer_load_dwordx4 v[140:143], v1, s[36:39], 0 offen offset:3072 nt
	buffer_load_dwordx4 v[144:147], v1, s[36:39], 0 offen offset:3584 nt
	s_movk_i32 s3, 0x160
	v_cmp_gt_u32_e32 vcc, s3, v0
	s_mov_b32 s3, 0x10000
	v_lshrrev_b32_e32 v227, 5, v0
	v_and_b32_e32 v228, 0x7c, v46
	v_add_u32_e32 v2, 0x200, v0
	v_lshrrev_b32_e32 v229, 5, v2
	v_mul_u32_u24_e32 v246, 0x110, v227
	v_lshl_add_u32 v246, v220, 3, v246
	v_add_u32_e32 v246, 0x10000, v246
	v_lshlrev_b32_e32 v247, 2, v46
	s_waitcnt vmcnt(17)
	v_cmp_ne_u32_e64 s[6:7], 0, v32
	v_cmp_ne_u32_e64 s[4:5], 0, v33
	v_cmp_eq_u32_e64 s[8:9], 0, v218
	s_nop 0
	s_and_saveexec_b64 s[12:13], s[8:9]
	s_cbranch_execz .LBB0_6
	s_bcnt1_i32_b64 s6, s[6:7]
	s_bcnt1_i32_b64 s4, s[4:5]
	v_mov_b32_e32 v1, 0x21100
	s_add_i32 s4, s4, s6
	v_lshl_add_u32 v1, v219, 2, v1
	v_mov_b32_e32 v2, s4
	ds_write_b32 v1, v2
